# speedup vs baseline: 1.0377x; 1.0107x over previous
.Lk2_epi:
	v_lshlrev_b32_e32 v180, 12, v171
	v_lshlrev_b32_e32 v181, 6, v172
	v_lshlrev_b32_e32 v182, 3, v173
	v_or3_b32 v181, v180, v181, v182
	v_add_u32_e32 v182, 0x800, v181
	v_cvt_pk_f16_f32 v184, v16, v17
	v_cvt_pk_f16_f32 v185, v18, v19
	v_cvt_pk_f16_f32 v186, v20, v21
	v_cvt_pk_f16_f32 v187, v22, v23
	v_cvt_pk_f16_f32 v188, v24, v25
	v_cvt_pk_f16_f32 v189, v26, v27
	v_cvt_pk_f16_f32 v190, v28, v29
	v_cvt_pk_f16_f32 v191, v30, v31
	ds_write2_b64 v181, v[184:185], v[186:187] offset1:2
	ds_write2_b64 v181, v[188:189], v[190:191] offset0:4 offset1:6
	v_cvt_pk_f16_f32 v184, v0, v1
	v_cvt_pk_f16_f32 v185, v2, v3
	v_cvt_pk_f16_f32 v186, v4, v5
	v_cvt_pk_f16_f32 v187, v6, v7
	v_cvt_pk_f16_f32 v188, v8, v9
	v_cvt_pk_f16_f32 v189, v10, v11
	v_cvt_pk_f16_f32 v190, v12, v13
	v_cvt_pk_f16_f32 v191, v14, v15
	ds_write2_b64 v182, v[184:185], v[186:187] offset1:2
	ds_write2_b64 v182, v[188:189], v[190:191] offset0:4 offset1:6
	s_lshl_b32 s36, s10, 18
	s_add_u32 s0, s6, s36
	s_addc_u32 s1, s7, 0
	s_lshl_b32 s36, s11, 3
	s_add_u32 s36, s36, s33
	s_lshl_b32 s36, s36, 12
	s_add_u32 s0, s0, s36
	s_addc_u32 s1, s1, 0
	v_or_b32_e32 v183, v180, v160
	s_waitcnt lgkmcnt(0)
	ds_read_b128 v[0:3], v183
	ds_read_b128 v[4:7], v183 offset:1024
	ds_read_b128 v[8:11], v183 offset:2048
	ds_read_b128 v[12:15], v183 offset:3072
	s_waitcnt lgkmcnt(3)
	global_store_dwordx4 v160, v[0:3], s[0:1] sc0 sc1
	s_waitcnt lgkmcnt(2)
	global_store_dwordx4 v160, v[4:7], s[0:1] offset:1024 sc0 sc1
	s_waitcnt lgkmcnt(1)
	global_store_dwordx4 v160, v[8:11], s[0:1] offset:2048 sc0 sc1
	s_waitcnt lgkmcnt(0)
	global_store_dwordx4 v160, v[12:15], s[0:1] offset:3072 sc0 sc1
	s_endpgm
